# speedup vs baseline: 1.0041x; 1.0022x over previous
.LBB1_9:
	v_add_u32_e32 v182, s20, v209
	ds_read_b64_tr_b16 v[178:179], v182 offset:24576
	ds_read_b64_tr_b16 v[180:181], v182 offset:25088
	s_waitcnt lgkmcnt(9)
	v_mfma_f32_32x32x16_f16 v[98:113], v[174:177], v[142:145], v[34:49]
	v_add_f32_e32 v82, v66, v67
	v_add_f32_e32 v82, v68, v82
	v_add_f32_e32 v82, v69, v82
	v_add_f32_e32 v82, v70, v82
	v_add_f32_e32 v82, v71, v82
	v_cvt_pk_f16_f32 v134, v66, v67
	v_cvt_pk_f16_f32 v135, v68, v69
	ds_read_b64_tr_b16 v[174:175], v182 offset:28672
	ds_read_b64_tr_b16 v[176:177], v182 offset:29184
	v_add_f32_e32 v66, v72, v82
	s_waitcnt lgkmcnt(10)
	v_mfma_f32_32x32x16_f16 v[82:97], v[170:173], v[142:145], v[34:49]
	v_add_f32_e32 v66, v73, v66
	v_add_f32_e32 v66, v74, v66
	v_add_f32_e32 v66, v75, v66
	v_cvt_pk_f16_f32 v136, v70, v71
	v_cvt_pk_f16_f32 v137, v72, v73
	ds_read_b64_tr_b16 v[170:171], v182 offset:25600
	ds_read_b64_tr_b16 v[172:173], v182 offset:26112
	s_waitcnt lgkmcnt(11)
	v_mfma_f32_32x32x16_f16 v[98:113], v[166:169], v[138:141], v[98:113]
	v_add_f32_e32 v66, v76, v66
	v_add_f32_e32 v66, v77, v66
	v_add_f32_e32 v66, v78, v66
	v_add_f32_e32 v66, v79, v66
	v_cvt_pk_f16_f32 v126, v74, v75
	v_cvt_pk_f16_f32 v127, v76, v77
	ds_read_b64_tr_b16 v[74:75], v182 offset:29696
	ds_read_b64_tr_b16 v[76:77], v182 offset:30208
	s_waitcnt lgkmcnt(12)
	v_mfma_f32_32x32x16_f16 v[82:97], v[162:165], v[138:141], v[82:97]
	v_add_f32_e32 v66, v80, v66
	v_add_f32_e32 v66, v81, v66
	v_add_f32_e32 v66, v50, v66
	v_add_f32_e32 v66, v51, v66
	v_cvt_pk_f16_f32 v128, v78, v79
	v_cvt_pk_f16_f32 v129, v80, v81
	ds_read_b64_tr_b16 v[70:71], v182 offset:26624
	ds_read_b64_tr_b16 v[72:73], v182 offset:27136
	s_waitcnt lgkmcnt(13)
	v_mfma_f32_32x32x16_f16 v[98:113], v[158:161], v[130:133], v[98:113]
	v_add_f32_e32 v66, v52, v66
	v_add_f32_e32 v66, v53, v66
	v_add_f32_e32 v66, v54, v66
	v_add_f32_e32 v78, v55, v66
	v_cvt_pk_f16_f32 v118, v50, v51
	v_cvt_pk_f16_f32 v119, v52, v53
	ds_read_b64_tr_b16 v[66:67], v182 offset:30720
	ds_read_b64_tr_b16 v[68:69], v182 offset:31232
	s_waitcnt lgkmcnt(14)
	v_mfma_f32_32x32x16_f16 v[82:97], v[154:157], v[130:133], v[82:97]
	v_add_f32_e32 v50, v56, v78
	v_add_f32_e32 v50, v57, v50
	v_add_f32_e32 v50, v58, v50
	v_add_f32_e32 v50, v59, v50
	v_cvt_pk_f16_f32 v120, v54, v55
	v_cvt_pk_f16_f32 v121, v56, v57
	ds_read_b64_tr_b16 v[54:55], v182 offset:27648
	ds_read_b64_tr_b16 v[56:57], v182 offset:28160
	s_waitcnt lgkmcnt(14)
	v_mfma_f32_32x32x16_f16 v[98:113], v[150:153], v[122:125], v[98:113]
	v_add_f32_e32 v50, v60, v50
	v_add_f32_e32 v50, v61, v50
	v_add_f32_e32 v50, v62, v50
	v_add_f32_e32 v78, v63, v50
	v_cvt_pk_f16_f32 v114, v58, v59
	v_cvt_pk_f16_f32 v115, v60, v61
	ds_read_b64_tr_b16 v[50:51], v182 offset:31744
	ds_read_b64_tr_b16 v[52:53], v182 offset:32256
	v_mfma_f32_32x32x16_f16 v[82:97], v[146:149], v[122:125], v[82:97]
	v_add_f32_e32 v58, v64, v78
	v_add_f32_e32 v58, v65, v58
	v_add_f32_e32 v58, 0, v58
	v_cvt_pk_f16_f32 v116, v62, v63
	v_cvt_pk_f16_f32 v117, v64, v65
	v_max_f32_e32 v59, v99, v99
	v_max_f32_e32 v60, v98, v98
	v_max_f32_e32 v59, v60, v59
	v_max3_f32 v60, v100, v101, v102
	v_max3_f32 v59, v59, v103, v104
	v_max3_f32 v60, v60, v105, v106
	v_max3_f32 v59, v59, v107, v108
	v_max3_f32 v60, v60, v109, v110
	v_max3_f32 v59, v59, v111, v112
	v_add_f32_e32 v182, v203, v58
	v_max3_f32 v60, v60, v113, v82
	v_max3_f32 v59, v59, v83, v84
	v_max3_f32 v60, v60, v85, v86
	v_max3_f32 v59, v59, v87, v88
	v_max3_f32 v60, v60, v89, v90
	v_max3_f32 v59, v59, v91, v92
	v_max3_f32 v60, v60, v93, v94
	v_max3_f32 v59, v59, v95, v96
	v_max3_f32 v58, v59, v60, v97
	v_mov_b32_e32 v59, v58
	s_nop 1
	v_permlane32_swap_b32_e32 v58, v59
	s_add_u32 s2, s16, 0xffffe000
	v_max_f32_e32 v59, v59, v59
	v_max_f32_e32 v58, v58, v58
	s_addc_u32 s3, s17, -1
	s_add_i32 s20, s24, s39
	s_mov_b32 s21, m0
	s_mov_b32 m0, s20
	s_nop 0
	global_load_lds_dwordx4 v211, s[2:3]
	s_mov_b32 m0, s21
	v_max_f32_e32 v58, v58, v59
	s_add_i32 s2, s22, s40
	s_mov_b32 s3, m0
	s_mov_b32 m0, s2
	s_nop 0
	global_load_lds_dwordx4 v211, s[18:19]
	s_mov_b32 m0, s3
	v_cmp_lt_f32_e32 vcc, s23, v58
	s_cmp_lg_u64 vcc, 0
	s_cselect_b64 s[2:3], -1, 0
	s_cbranch_vccnz .LBB1_17

.LBB1_12:
	s_add_i32 s2, s22, 0x2000
	s_cmpk_lg_i32 s22, 0x4000
	s_cselect_b32 s43, s2, 0
	v_add_u32_e32 v183, s24, v209
	ds_read_b64_tr_b16 v[154:155], v183 offset:24576
	ds_read_b64_tr_b16 v[156:157], v183 offset:25088
	s_waitcnt lgkmcnt(9)
	v_mfma_f32_32x32x16_f16 v[66:81], v[58:61], v[142:145], v[34:49]
	v_add_f32_e32 v50, v98, v99
	v_add_f32_e32 v50, v100, v50
	v_add_f32_e32 v50, v101, v50
	v_add_f32_e32 v50, v102, v50
	v_add_f32_e32 v50, v103, v50
	v_cvt_pk_f16_f32 v134, v98, v99
	v_cvt_pk_f16_f32 v135, v100, v101
	ds_read_b64_tr_b16 v[150:151], v183 offset:28672
	ds_read_b64_tr_b16 v[152:153], v183 offset:29184
	v_add_f32_e32 v50, v104, v50
	v_add_f32_e32 v50, v105, v50
	v_add_f32_e32 v50, v106, v50
	v_add_f32_e32 v98, v107, v50
	s_waitcnt lgkmcnt(10)
	v_mfma_f32_32x32x16_f16 v[50:65], v[146:149], v[142:145], v[34:49]
	v_cvt_pk_f16_f32 v136, v102, v103
	v_cvt_pk_f16_f32 v137, v104, v105
	ds_read_b64_tr_b16 v[146:147], v183 offset:25600
	ds_read_b64_tr_b16 v[148:149], v183 offset:26112
	s_waitcnt lgkmcnt(11)
	v_mfma_f32_32x32x16_f16 v[66:81], v[178:181], v[138:141], v[66:81]
	v_add_f32_e32 v98, v108, v98
	v_add_f32_e32 v98, v109, v98
	v_add_f32_e32 v98, v110, v98
	v_add_f32_e32 v98, v111, v98
	v_cvt_pk_f16_f32 v126, v106, v107
	v_cvt_pk_f16_f32 v127, v108, v109
	ds_read_b64_tr_b16 v[106:107], v183 offset:29696
	ds_read_b64_tr_b16 v[108:109], v183 offset:30208
	s_waitcnt lgkmcnt(12)
	v_mfma_f32_32x32x16_f16 v[50:65], v[170:173], v[138:141], v[50:65]
	v_add_f32_e32 v98, v112, v98
	v_add_f32_e32 v98, v113, v98
	v_add_f32_e32 v98, v82, v98
	v_add_f32_e32 v98, v83, v98
	v_cvt_pk_f16_f32 v128, v110, v111
	v_cvt_pk_f16_f32 v129, v112, v113
	ds_read_b64_tr_b16 v[102:103], v183 offset:26624
	ds_read_b64_tr_b16 v[104:105], v183 offset:27136
	s_waitcnt lgkmcnt(13)
	v_mfma_f32_32x32x16_f16 v[66:81], v[174:177], v[130:133], v[66:81]
	v_add_f32_e32 v98, v84, v98
	v_add_f32_e32 v98, v85, v98
	v_add_f32_e32 v98, v86, v98
	v_add_f32_e32 v110, v87, v98
	v_cvt_pk_f16_f32 v118, v82, v83
	v_cvt_pk_f16_f32 v119, v84, v85
	ds_read_b64_tr_b16 v[98:99], v183 offset:30720
	ds_read_b64_tr_b16 v[100:101], v183 offset:31232
	s_waitcnt lgkmcnt(14)
	v_mfma_f32_32x32x16_f16 v[50:65], v[162:165], v[130:133], v[50:65]
	v_add_f32_e32 v82, v88, v110
	v_add_f32_e32 v82, v89, v82
	v_add_f32_e32 v82, v90, v82
	v_add_f32_e32 v82, v91, v82
	v_cvt_pk_f16_f32 v120, v86, v87
	v_cvt_pk_f16_f32 v121, v88, v89
	ds_read_b64_tr_b16 v[86:87], v183 offset:27648
	ds_read_b64_tr_b16 v[88:89], v183 offset:28160
	s_waitcnt lgkmcnt(14)
	v_mfma_f32_32x32x16_f16 v[66:81], v[166:169], v[122:125], v[66:81]
	v_add_f32_e32 v82, v92, v82
	v_add_f32_e32 v82, v93, v82
	v_add_f32_e32 v82, v94, v82
	v_add_f32_e32 v110, v95, v82
	v_cvt_pk_f16_f32 v114, v90, v91
	v_cvt_pk_f16_f32 v115, v92, v93
	ds_read_b64_tr_b16 v[82:83], v183 offset:31744
	ds_read_b64_tr_b16 v[84:85], v183 offset:32256
	v_mfma_f32_32x32x16_f16 v[50:65], v[158:161], v[122:125], v[50:65]
	v_add_f32_e32 v90, v96, v110
	v_add_f32_e32 v90, v97, v90
	v_add_f32_e32 v90, 0, v90
	v_cvt_pk_f16_f32 v116, v94, v95
	v_cvt_pk_f16_f32 v117, v96, v97
	v_max_f32_e32 v91, v67, v67
	v_max_f32_e32 v92, v66, v66
	v_max_f32_e32 v91, v92, v91
	v_max3_f32 v92, v68, v69, v70
	v_max3_f32 v91, v91, v71, v72
	v_max3_f32 v92, v92, v73, v74
	v_max3_f32 v91, v91, v75, v76
	v_max3_f32 v92, v92, v77, v78
	v_max3_f32 v91, v91, v79, v80
	v_add_f32_e32 v203, v182, v90
	v_max3_f32 v92, v92, v81, v50
	v_max3_f32 v91, v91, v51, v52
	v_max3_f32 v92, v92, v53, v54
	v_max3_f32 v91, v91, v55, v56
	v_max3_f32 v92, v92, v57, v58
	v_max3_f32 v91, v91, v59, v60
	v_max3_f32 v92, v92, v61, v62
	v_max3_f32 v91, v91, v63, v64
	v_max3_f32 v90, v91, v92, v65
	v_mov_b32_e32 v91, v90
	s_nop 1
	v_permlane32_swap_b32_e32 v90, v91
	s_add_i32 s2, s22, s39
	v_max_f32_e32 v91, v91, v91
	v_max_f32_e32 v90, v90, v90
	s_mov_b32 s3, m0
	s_mov_b32 m0, s2
	s_nop 0
	global_load_lds_dwordx4 v211, s[16:17]
	s_mov_b32 m0, s3
	s_add_u32 s2, s18, 0x2000
	v_max_f32_e32 v90, v90, v91
	s_addc_u32 s3, s19, 0
	s_add_i32 s20, s43, s40
	s_mov_b32 s21, m0
	s_mov_b32 m0, s20
	s_nop 0
	global_load_lds_dwordx4 v211, s[2:3]
	s_mov_b32 m0, s21
	v_cmp_lt_f32_e32 vcc, s23, v90
	s_cmp_lg_u64 vcc, 0
	s_cselect_b64 s[2:3], -1, 0
	s_cbranch_vccnz .LBB1_20

.LBB1_87:
	v_add_u32_e32 v65, s6, v251
	ds_read_b64_tr_b16 v[192:193], v65
	ds_read_b64_tr_b16 v[194:195], v65 offset:512
	s_waitcnt lgkmcnt(9)
	v_mfma_f32_32x32x16_f16 v[112:127], v[188:191], v[140:143], v[32:47]
	v_add_f32_e32 v66, v80, v81
	v_add_f32_e32 v66, v82, v66
	v_add_f32_e32 v66, v83, v66
	v_add_f32_e32 v66, v84, v66
	v_add_f32_e32 v66, v85, v66
	v_cvt_pk_f16_f32 v156, v80, v81
	v_cvt_pk_f16_f32 v157, v82, v83
	ds_read_b64_tr_b16 v[188:189], v65 offset:4096
	ds_read_b64_tr_b16 v[190:191], v65 offset:4608
	s_waitcnt lgkmcnt(10)
	v_mfma_f32_32x32x16_f16 v[96:111], v[184:187], v[140:143], v[32:47]
	v_add_f32_e32 v66, v86, v66
	v_add_f32_e32 v66, v87, v66
	v_add_f32_e32 v66, v88, v66
	v_add_f32_e32 v66, v89, v66
	v_cvt_pk_f16_f32 v158, v84, v85
	v_cvt_pk_f16_f32 v159, v86, v87
	ds_read_b64_tr_b16 v[78:79], v65 offset:1024
	ds_read_b64_tr_b16 v[80:81], v65 offset:1536
	s_waitcnt lgkmcnt(11)
	v_mfma_f32_32x32x16_f16 v[112:127], v[180:183], v[136:139], v[112:127]
	v_add_f32_e32 v66, v90, v66
	v_add_f32_e32 v66, v91, v66
	v_add_f32_e32 v66, v92, v66
	v_add_f32_e32 v66, v93, v66
	v_cvt_pk_f16_f32 v152, v88, v89
	v_cvt_pk_f16_f32 v153, v90, v91
	ds_read_b64_tr_b16 v[74:75], v65 offset:5120
	ds_read_b64_tr_b16 v[76:77], v65 offset:5632
	s_waitcnt lgkmcnt(12)
	v_mfma_f32_32x32x16_f16 v[96:111], v[176:179], v[136:139], v[96:111]
	v_add_f32_e32 v66, v94, v66
	v_add_f32_e32 v66, v95, v66
	v_add_f32_e32 v66, v48, v66
	v_add_f32_e32 v66, v49, v66
	v_cvt_pk_f16_f32 v154, v92, v93
	v_cvt_pk_f16_f32 v155, v94, v95
	ds_read_b64_tr_b16 v[70:71], v65 offset:2048
	ds_read_b64_tr_b16 v[72:73], v65 offset:2560
	s_waitcnt lgkmcnt(13)
	v_mfma_f32_32x32x16_f16 v[112:127], v[172:175], v[132:135], v[112:127]
	v_add_f32_e32 v66, v50, v66
	v_add_f32_e32 v66, v51, v66
	v_add_f32_e32 v66, v52, v66
	v_add_f32_e32 v82, v53, v66
	v_cvt_pk_f16_f32 v148, v48, v49
	v_cvt_pk_f16_f32 v149, v50, v51
	ds_read_b64_tr_b16 v[66:67], v65 offset:6144
	ds_read_b64_tr_b16 v[68:69], v65 offset:6656
	s_waitcnt lgkmcnt(14)
	v_mfma_f32_32x32x16_f16 v[96:111], v[168:171], v[132:135], v[96:111]
	v_add_f32_e32 v48, v54, v82
	v_add_f32_e32 v48, v55, v48
	v_add_f32_e32 v48, v56, v48
	v_add_f32_e32 v48, v57, v48
	v_cvt_pk_f16_f32 v150, v52, v53
	v_cvt_pk_f16_f32 v151, v54, v55
	ds_read_b64_tr_b16 v[52:53], v65 offset:3072
	ds_read_b64_tr_b16 v[54:55], v65 offset:3584
	s_waitcnt lgkmcnt(14)
	v_mfma_f32_32x32x16_f16 v[112:127], v[164:167], v[128:131], v[112:127]
	v_add_f32_e32 v48, v58, v48
	v_add_f32_e32 v48, v59, v48
	v_add_f32_e32 v48, v60, v48
	v_add_f32_e32 v82, v61, v48
	v_cvt_pk_f16_f32 v144, v56, v57
	v_cvt_pk_f16_f32 v145, v58, v59
	ds_read_b64_tr_b16 v[48:49], v65 offset:7168
	ds_read_b64_tr_b16 v[50:51], v65 offset:7680
	v_mfma_f32_32x32x16_f16 v[96:111], v[160:163], v[128:131], v[96:111]
	v_add_f32_e32 v56, v62, v82
	v_add_f32_e32 v56, v63, v56
	v_add_f32_e32 v56, 0, v56
	v_cvt_pk_f16_f32 v146, v60, v61
	v_cvt_pk_f16_f32 v147, v62, v63
	v_max_f32_e32 v57, v113, v113
	v_max_f32_e32 v58, v112, v112
	v_max_f32_e32 v57, v58, v57
	v_max3_f32 v58, v114, v115, v116
	v_max3_f32 v57, v57, v117, v118
	v_max3_f32 v58, v58, v119, v120
	v_max3_f32 v57, v57, v121, v122
	v_max3_f32 v58, v58, v123, v124
	v_max3_f32 v57, v57, v125, v126
	v_add_f32_e32 v64, v64, v56
	v_max3_f32 v58, v58, v127, v96
	v_max3_f32 v57, v57, v97, v98
	v_max3_f32 v58, v58, v99, v100
	v_max3_f32 v57, v57, v101, v102
	v_max3_f32 v58, v58, v103, v104
	v_max3_f32 v57, v57, v105, v106
	v_max3_f32 v58, v58, v107, v108
	v_max3_f32 v57, v57, v109, v110
	v_max3_f32 v56, v57, v58, v111
	v_mov_b32_e32 v57, v56
	s_add_u32 s6, s4, 0xffffe000
	s_nop 0
	v_permlane32_swap_b32_e32 v56, v57
	s_addc_u32 s7, s5, -1
	s_add_i32 s8, s30, s22
	v_max_f32_e32 v57, v57, v57
	v_max_f32_e32 v56, v56, v56
	s_mov_b32 s9, m0
	s_mov_b32 m0, s8
	s_nop 0
	global_load_lds_dwordx4 v211, s[6:7]
	s_mov_b32 m0, s9
	s_add_u32 s6, s2, 0xffffe000
	v_max_f32_e32 v56, v56, v57
	s_addc_u32 s7, s3, -1
	s_add_i32 s8, s12, s23
	s_mov_b32 s9, m0
	s_mov_b32 m0, s8
	s_nop 0
	global_load_lds_dwordx4 v211, s[6:7]
	s_mov_b32 m0, s9
	v_cmp_lt_f32_e32 vcc, s17, v56
	s_cmp_lg_u64 vcc, 0
	s_cselect_b64 s[6:7], -1, 0
	s_cbranch_vccnz .LBB1_95

.LBB1_90:
	s_add_i32 s6, s12, 0x2000
	s_cmpk_lg_i32 s12, 0x4000
	s_cselect_b32 s25, s6, 0
	v_add_u32_e32 v65, s30, v251
	ds_read_b64_tr_b16 v[168:169], v65
	ds_read_b64_tr_b16 v[170:171], v65 offset:512
	s_waitcnt lgkmcnt(9)
	v_mfma_f32_32x32x16_f16 v[80:95], v[56:59], v[140:143], v[32:47]
	v_add_f32_e32 v48, v112, v113
	v_add_f32_e32 v48, v114, v48
	v_add_f32_e32 v48, v115, v48
	v_add_f32_e32 v48, v116, v48
	v_add_f32_e32 v48, v117, v48
	v_cvt_pk_f16_f32 v156, v112, v113
	v_cvt_pk_f16_f32 v157, v114, v115
	ds_read_b64_tr_b16 v[164:165], v65 offset:4096
	ds_read_b64_tr_b16 v[166:167], v65 offset:4608
	v_add_f32_e32 v48, v118, v48
	v_add_f32_e32 v48, v119, v48
	v_add_f32_e32 v48, v120, v48
	v_add_f32_e32 v66, v121, v48
	s_waitcnt lgkmcnt(10)
	v_mfma_f32_32x32x16_f16 v[48:63], v[160:163], v[140:143], v[32:47]
	v_cvt_pk_f16_f32 v158, v116, v117
	v_cvt_pk_f16_f32 v159, v118, v119
	ds_read_b64_tr_b16 v[160:161], v65 offset:1024
	ds_read_b64_tr_b16 v[162:163], v65 offset:1536
	s_waitcnt lgkmcnt(11)
	v_mfma_f32_32x32x16_f16 v[80:95], v[188:191], v[136:139], v[80:95]
	v_add_f32_e32 v66, v122, v66
	v_add_f32_e32 v66, v123, v66
	v_add_f32_e32 v66, v124, v66
	v_add_f32_e32 v66, v125, v66
	v_cvt_pk_f16_f32 v152, v120, v121
	v_cvt_pk_f16_f32 v153, v122, v123
	ds_read_b64_tr_b16 v[116:117], v65 offset:5120
	ds_read_b64_tr_b16 v[118:119], v65 offset:5632
	s_waitcnt lgkmcnt(12)
	v_mfma_f32_32x32x16_f16 v[48:63], v[184:187], v[136:139], v[48:63]
	v_add_f32_e32 v66, v126, v66
	v_add_f32_e32 v66, v127, v66
	v_add_f32_e32 v66, v96, v66
	v_add_f32_e32 v66, v97, v66
	v_cvt_pk_f16_f32 v154, v124, v125
	v_cvt_pk_f16_f32 v155, v126, v127
	ds_read_b64_tr_b16 v[112:113], v65 offset:2048
	ds_read_b64_tr_b16 v[114:115], v65 offset:2560
	s_waitcnt lgkmcnt(13)
	v_mfma_f32_32x32x16_f16 v[80:95], v[74:77], v[132:135], v[80:95]
	v_add_f32_e32 v66, v98, v66
	v_add_f32_e32 v66, v99, v66
	v_add_f32_e32 v66, v100, v66
	v_add_f32_e32 v66, v101, v66
	v_cvt_pk_f16_f32 v148, v96, v97
	v_cvt_pk_f16_f32 v149, v98, v99
	ds_read_b64_tr_b16 v[74:75], v65 offset:6144
	ds_read_b64_tr_b16 v[76:77], v65 offset:6656
	s_waitcnt lgkmcnt(14)
	v_mfma_f32_32x32x16_f16 v[48:63], v[176:179], v[132:135], v[48:63]
	v_add_f32_e32 v66, v102, v66
	v_add_f32_e32 v66, v103, v66
	v_add_f32_e32 v66, v104, v66
	v_add_f32_e32 v66, v105, v66
	v_cvt_pk_f16_f32 v150, v100, v101
	v_cvt_pk_f16_f32 v151, v102, v103
	ds_read_b64_tr_b16 v[70:71], v65 offset:3072
	ds_read_b64_tr_b16 v[72:73], v65 offset:3584
	s_waitcnt lgkmcnt(14)
	v_mfma_f32_32x32x16_f16 v[80:95], v[180:183], v[128:131], v[80:95]
	v_add_f32_e32 v66, v106, v66
	v_add_f32_e32 v66, v107, v66
	v_add_f32_e32 v66, v108, v66
	v_add_f32_e32 v78, v109, v66
	v_cvt_pk_f16_f32 v144, v104, v105
	v_cvt_pk_f16_f32 v145, v106, v107
	ds_read_b64_tr_b16 v[66:67], v65 offset:7168
	ds_read_b64_tr_b16 v[68:69], v65 offset:7680
	v_mfma_f32_32x32x16_f16 v[48:63], v[172:175], v[128:131], v[48:63]
	v_add_f32_e32 v65, v110, v78
	v_add_f32_e32 v65, v111, v65
	v_add_f32_e32 v65, 0, v65
	v_cvt_pk_f16_f32 v146, v108, v109
	v_cvt_pk_f16_f32 v147, v110, v111
	v_max_f32_e32 v78, v81, v81
	v_max_f32_e32 v79, v80, v80
	v_max_f32_e32 v78, v79, v78
	v_max3_f32 v79, v82, v83, v84
	v_max3_f32 v78, v78, v85, v86
	v_max3_f32 v79, v79, v87, v88
	v_max3_f32 v78, v78, v89, v90
	v_max3_f32 v79, v79, v91, v92
	v_max3_f32 v78, v78, v93, v94
	v_add_f32_e32 v64, v64, v65
	v_max3_f32 v79, v79, v95, v48
	v_max3_f32 v78, v78, v49, v50
	v_max3_f32 v79, v79, v51, v52
	v_max3_f32 v78, v78, v53, v54
	v_max3_f32 v79, v79, v55, v56
	v_max3_f32 v78, v78, v57, v58
	v_max3_f32 v79, v79, v59, v60
	v_max3_f32 v78, v78, v61, v62
	v_max3_f32 v65, v78, v79, v63
	v_mov_b32_e32 v78, v65
	s_nop 1
	v_permlane32_swap_b32_e32 v65, v78
	v_max_f32_e32 v78, v78, v78
	v_max_f32_e32 v65, v65, v65
	s_add_i32 s6, s12, s22
	s_mov_b32 s7, m0
	s_mov_b32 m0, s6
	s_nop 0
	global_load_lds_dwordx4 v211, s[4:5]
	s_mov_b32 m0, s7
	v_max_f32_e32 v65, v65, v78
	s_add_i32 s6, s25, s23
	s_mov_b32 s7, m0
	s_mov_b32 m0, s6
	s_nop 0
	global_load_lds_dwordx4 v211, s[2:3]
	s_mov_b32 m0, s7
	v_cmp_lt_f32_e32 vcc, s17, v65
	s_cmp_lg_u64 vcc, 0
	s_cselect_b64 s[6:7], -1, 0
	s_cbranch_vccnz .LBB1_98
